# P5 epilogue: v_nop replaced by reordering two independent packed FMAs, store addresses as 32-bit offsets from the scalar base (1 VALU per store instead of 5); never-executed pad keeps later code at th
# speedup vs baseline: 1.0347x; 1.0000x over previous
; #define PG8_LAS __attribute__((address_space(3)))
;     __device__ __forceinline__ void operator()(const i32x4 (&acc)[2][2][4][2], const Unit& u, int wr, int wc, int fr, int fq, PG8_LAS unsigned* scr) const {
;         const int j = u.pn & 7;
;         const int row0 = u.pm * BM + wr * 64 + fr, c0 = j * 128 + wc * 32 + 8 * fq, cl = wc * 32 + 8 * fq;
;         f32x4 bgv[2], buv[2], csg[2], csu[2];
;         constexpr float C2 = 1.702f * 1.44269504f;
; #pragma unroll
;         for (int n = 0; n < 2; ++n) { bgv[n] = *(const PG8_LAS f32x4*)(scr + 512 + cl + 4 * n) * C2; buv[n] = *(const PG8_LAS f32x4*)(scr + 512 + 128 + cl + 4 * n);
;             csg[n] = *(const PG8_LAS f32x4*)(scr + 256 + cl + 4 * n) * (C2 / 127.0f); csu[n] = *(const PG8_LAS f32x4*)(scr + 256 + 128 + cl + 4 * n) * (1.0f / 127.0f); }
; #pragma unroll
;         for (int ai = 0; ai < 2; ++ai)
; #pragma unroll
;             for (int mp = 0; mp < 4; mp += 2) { unsigned wp[2][2];
; #pragma unroll
;                 for (int hm = 0; hm < 2; ++hm) { const int m = mp + hm; const int r = ai * HALF + wr * 64 + m * 16 + fr; const float rs = __uint_as_float(scr[r]); float o[8];
; #pragma unroll
;                     for (int n = 0; n < 2; ++n) { const f32x4 sgr = csg[n] * rs, sur = csu[n] * rs;
; #pragma unroll
;                         for (int q = 0; q < 4; ++q) { const float h = fminf(__builtin_fmaf((float)acc[ai][0][m][n][q], sgr[q], bgv[n][q]), 7.0f * C2), up = fminf(fmaxf(__builtin_fmaf((float)acc[ai][1][m][n][q], sur[q], buv[n][q]), -7.0f), 7.0f);
;                             const float sg = __builtin_amdgcn_rcpf(1.0f + __builtin_amdgcn_exp2f(-h)); o[4 * n + q] = __builtin_fmaf(up, ACT_SC / C2, ACT_SC / C2) * (h * sg); } }
;                     int w0 = __builtin_amdgcn_cvt_pk_fp8_f32(o[0], o[1], 0, false); w0 = __builtin_amdgcn_cvt_pk_fp8_f32(o[2], o[3], w0, true);
;                     int w1 = __builtin_amdgcn_cvt_pk_fp8_f32(o[4], o[5], 0, false); w1 = __builtin_amdgcn_cvt_pk_fp8_f32(o[6], o[7], w1, true);
;                     wp[hm][0] = (unsigned)w0; wp[hm][1] = (unsigned)w1; }
.LBB0_807:
	v_ashrrev_i32_e32 v185, 2, v168
	v_and_b32_e32 v185, 0xffffffc0, v185
	v_bfe_u32 v201, v168, 4, 2
	v_lshrrev_b32_e32 v208, 1, v168
	v_and_b32_e32 v208, 0x60, v208
	v_lshl_or_b32 v208, v201, 3, v208
	s_lshl_b32 s10, s39, 7
	s_and_b32 s10, s10, 0x380
	v_and_b32_e32 v201, 1, v201
	v_lshlrev_b32_e32 v207, 3, v201
	v_add_u32_e32 v206, s10, v208
	v_sub_u32_e32 v206, v206, v207
	v_mov_b32_e32 v207, 0
	v_lshlrev_b32_e32 v201, 4, v201
	v_lshlrev_b32_e32 v208, 2, v208
	v_readlane_b32 s10, v255, 5
	v_and_b32_e32 v160, 15, v168
	v_lshl_add_u32 v161, v185, 2, 0
	v_lshl_add_u32 v161, v160, 2, v161
	v_add_u32_e32 v161, s10, v161
	ds_read2_b32 v[152:153], v161 offset0:0 offset1:16
	ds_read2_b32 v[154:155], v161 offset0:32 offset1:48
	ds_read2_b32 v[156:157], v161 offset0:128 offset1:144
	ds_read2_b32 v[158:159], v161 offset0:160 offset1:176
	v_lshl_add_u32 v185, s40, 8, v185
	v_or_b32_e32 v185, v185, v160
	v_add_u32_e32 v185, v185, v201
	v_lshl_add_u32 v207, v185, 10, v206
	s_mov_b32 s100, 0x405083aa
	s_mov_b32 s101, 0x405083aa
	v_add_u32_e32 v160, 0x21100, v208
	ds_read_b128 v[136:139], v160
	v_add_u32_e32 v160, 0x21300, v208
	ds_read_b128 v[140:143], v160
	v_add_u32_e32 v160, 0x20d00, v208
	ds_read_b128 v[144:147], v160
	v_add_u32_e32 v160, 0x20f00, v208
	ds_read_b128 v[148:151], v160
	s_waitcnt lgkmcnt(0)
	v_mul_f32_e32 v136, 0x401d265f, v136
	v_mul_f32_e32 v137, 0x401d265f, v137
	v_mul_f32_e32 v138, 0x401d265f, v138
	v_mul_f32_e32 v139, 0x401d265f, v139
	v_mul_f32_e32 v144, 0x3c9e6325, v144
	v_mul_f32_e32 v145, 0x3c9e6325, v145
	v_mul_f32_e32 v146, 0x3c9e6325, v146
	v_mul_f32_e32 v147, 0x3c9e6325, v147
	v_mul_f32_e32 v148, 0x3c010204, v148
	v_mul_f32_e32 v149, 0x3c010204, v149
	v_mul_f32_e32 v150, 0x3c010204, v150
	v_mul_f32_e32 v151, 0x3c010204, v151
	v_cvt_f32_i32_e32 v128, v128
	v_cvt_f32_i32_e32 v129, v129
	v_cvt_f32_i32_e32 v130, v130
	v_cvt_f32_i32_e32 v131, v131
	v_cvt_f32_i32_e32 v132, v132
	v_cvt_f32_i32_e32 v133, v133
	v_cvt_f32_i32_e32 v134, v134
	v_cvt_f32_i32_e32 v135, v135
	v_pk_mul_f32 v[160:161], v[144:145], v[152:153] op_sel_hi:[1,0]
	v_pk_mul_f32 v[162:163], v[146:147], v[152:153] op_sel_hi:[1,0]
	v_pk_fma_f32 v[128:129], v[128:129], v[160:161], v[136:137]
	v_pk_fma_f32 v[130:131], v[130:131], v[162:163], v[138:139]
	v_pk_mul_f32 v[160:161], v[148:149], v[152:153] op_sel_hi:[1,0]
	v_pk_mul_f32 v[162:163], v[150:151], v[152:153] op_sel_hi:[1,0]
	v_min_f32_e32 v128, 0x41898193, v128
	v_min_f32_e32 v129, 0x41898193, v129
	v_min_f32_e32 v130, 0x41898193, v130
	v_min_f32_e32 v131, 0x41898193, v131
	v_pk_fma_f32 v[132:133], v[132:133], v[160:161], v[140:141]
	v_pk_fma_f32 v[134:135], v[134:135], v[162:163], v[142:143]
	v_exp_f32_e64 v160, -v128
	v_exp_f32_e64 v161, -v129
	v_exp_f32_e64 v162, -v130
	v_exp_f32_e64 v163, -v131
	v_med3_f32 v132, v132, s8, v199
	v_med3_f32 v133, v133, s8, v199
	v_med3_f32 v134, v134, s8, v199
	v_med3_f32 v135, v135, s8, v199
	v_pk_add_f32 v[160:161], v[160:161], 1.0 op_sel_hi:[1,0]
	v_pk_add_f32 v[162:163], v[162:163], 1.0 op_sel_hi:[1,0]
	v_rcp_f32_e32 v160, v160
	v_rcp_f32_e32 v161, v161
	v_rcp_f32_e32 v162, v162
	v_rcp_f32_e32 v163, v163
	v_pk_fma_f32 v[132:133], v[132:133], s[100:101], s[100:101]
	v_pk_fma_f32 v[134:135], v[134:135], s[100:101], s[100:101]
	v_pk_mul_f32 v[128:129], v[128:129], v[160:161]
	v_pk_mul_f32 v[130:131], v[130:131], v[162:163]
	v_pk_mul_f32 v[128:129], v[132:133], v[128:129]
	v_pk_mul_f32 v[130:131], v[134:135], v[130:131]
	v_cvt_pk_fp8_f32 v128, v128, v129
	v_cvt_pk_fp8_f32 v128, v130, v131 op_sel:[0,0,1]
	s_and_b64 vcc, exec, s[62:63]
	s_cbranch_vccz .Lp5_epi_nobar
	s_barrier
.Lp5_epi_nobar:
	v_cvt_f32_i32_e32 v112, v112
	v_cvt_f32_i32_e32 v113, v113
	v_cvt_f32_i32_e32 v114, v114
	v_cvt_f32_i32_e32 v115, v115
	v_cvt_f32_i32_e32 v116, v116
	v_cvt_f32_i32_e32 v117, v117
	v_cvt_f32_i32_e32 v118, v118
	v_cvt_f32_i32_e32 v119, v119
	v_pk_mul_f32 v[202:203], v[144:145], v[152:153] op_sel:[0,1] op_sel_hi:[1,1]
	v_pk_mul_f32 v[204:205], v[146:147], v[152:153] op_sel:[0,1] op_sel_hi:[1,1]
	v_pk_fma_f32 v[112:113], v[112:113], v[202:203], v[136:137]
	v_pk_fma_f32 v[114:115], v[114:115], v[204:205], v[138:139]
	v_pk_mul_f32 v[202:203], v[148:149], v[152:153] op_sel:[0,1] op_sel_hi:[1,1]
	v_pk_mul_f32 v[204:205], v[150:151], v[152:153] op_sel:[0,1] op_sel_hi:[1,1]
	v_min_f32_e32 v112, 0x41898193, v112
	v_min_f32_e32 v113, 0x41898193, v113
	v_min_f32_e32 v114, 0x41898193, v114
	v_min_f32_e32 v115, 0x41898193, v115
	v_pk_fma_f32 v[116:117], v[116:117], v[202:203], v[140:141]
	v_pk_fma_f32 v[118:119], v[118:119], v[204:205], v[142:143]
	v_exp_f32_e64 v202, -v112
	v_exp_f32_e64 v203, -v113
	v_exp_f32_e64 v204, -v114
	v_exp_f32_e64 v205, -v115
	v_med3_f32 v116, v116, s8, v199
	v_med3_f32 v117, v117, s8, v199
	v_med3_f32 v118, v118, s8, v199
	v_med3_f32 v119, v119, s8, v199
	v_pk_add_f32 v[202:203], v[202:203], 1.0 op_sel_hi:[1,0]
	v_pk_add_f32 v[204:205], v[204:205], 1.0 op_sel_hi:[1,0]
	v_rcp_f32_e32 v202, v202
	v_rcp_f32_e32 v203, v203
	v_rcp_f32_e32 v204, v204
	v_rcp_f32_e32 v205, v205
	v_pk_fma_f32 v[116:117], v[116:117], s[100:101], s[100:101]
	v_pk_fma_f32 v[118:119], v[118:119], s[100:101], s[100:101]
	v_pk_mul_f32 v[112:113], v[112:113], v[202:203]
	v_pk_mul_f32 v[114:115], v[114:115], v[204:205]
	v_pk_mul_f32 v[112:113], v[116:117], v[112:113]
	v_pk_mul_f32 v[114:115], v[118:119], v[114:115]
	v_cvt_pk_fp8_f32 v130, v112, v113
	v_cvt_pk_fp8_f32 v130, v114, v115 op_sel:[0,0,1]
	v_cvt_f32_i32_e32 v96, v96
	v_cvt_f32_i32_e32 v97, v97
	v_cvt_f32_i32_e32 v98, v98
	v_cvt_f32_i32_e32 v99, v99
	v_cvt_f32_i32_e32 v100, v100
	v_cvt_f32_i32_e32 v101, v101
	v_cvt_f32_i32_e32 v102, v102
;     __device__ __forceinline__ void operator()(const i32x4 (&acc)[2][2][4][2], const Unit& u, int wr, int wc, int fr, int fq, PG8_LAS unsigned* scr) const {
;     ...
;                 for (int hm = 0; hm < 2; ++hm) { const int m = mp + hm; const int r = ai * HALF + wr * 64 + m * 16 + fr; const float rs = __uint_as_float(scr[r]); float o[8];
; #pragma unroll
;                     for (int n = 0; n < 2; ++n) { const f32x4 sgr = csg[n] * rs, sur = csu[n] * rs;
; #pragma unroll
;                         for (int q = 0; q < 4; ++q) { const float h = fminf(__builtin_fmaf((float)acc[ai][0][m][n][q], sgr[q], bgv[n][q]), 7.0f * C2), up = fminf(fmaxf(__builtin_fmaf((float)acc[ai][1][m][n][q], sur[q], buv[n][q]), -7.0f), 7.0f);
;                             const float sg = __builtin_amdgcn_rcpf(1.0f + __builtin_amdgcn_exp2f(-h)); o[4 * n + q] = __builtin_fmaf(up, ACT_SC / C2, ACT_SC / C2) * (h * sg); } }
;                     int w0 = __builtin_amdgcn_cvt_pk_fp8_f32(o[0], o[1], 0, false); w0 = __builtin_amdgcn_cvt_pk_fp8_f32(o[2], o[3], w0, true);
;                     int w1 = __builtin_amdgcn_cvt_pk_fp8_f32(o[4], o[5], 0, false); w1 = __builtin_amdgcn_cvt_pk_fp8_f32(o[6], o[7], w1, true);
;                     wp[hm][0] = (unsigned)w0; wp[hm][1] = (unsigned)w1; }
	v_cvt_f32_i32_e32 v103, v103
	v_pk_mul_f32 v[160:161], v[144:145], v[154:155] op_sel_hi:[1,0]
	v_pk_mul_f32 v[162:163], v[146:147], v[154:155] op_sel_hi:[1,0]
	v_pk_fma_f32 v[96:97], v[96:97], v[160:161], v[136:137]
	v_pk_fma_f32 v[98:99], v[98:99], v[162:163], v[138:139]
	v_pk_mul_f32 v[160:161], v[148:149], v[154:155] op_sel_hi:[1,0]
	v_pk_mul_f32 v[162:163], v[150:151], v[154:155] op_sel_hi:[1,0]
	v_min_f32_e32 v96, 0x41898193, v96
	v_min_f32_e32 v97, 0x41898193, v97
	v_min_f32_e32 v98, 0x41898193, v98
	v_min_f32_e32 v99, 0x41898193, v99
	v_pk_fma_f32 v[100:101], v[100:101], v[160:161], v[140:141]
	v_pk_fma_f32 v[102:103], v[102:103], v[162:163], v[142:143]
	v_exp_f32_e64 v160, -v96
	v_exp_f32_e64 v161, -v97
	v_exp_f32_e64 v162, -v98
	v_exp_f32_e64 v163, -v99
	v_med3_f32 v100, v100, s8, v199
	v_med3_f32 v101, v101, s8, v199
	v_med3_f32 v102, v102, s8, v199
	v_med3_f32 v103, v103, s8, v199
	v_pk_add_f32 v[160:161], v[160:161], 1.0 op_sel_hi:[1,0]
	v_pk_add_f32 v[162:163], v[162:163], 1.0 op_sel_hi:[1,0]
	v_rcp_f32_e32 v160, v160
	v_rcp_f32_e32 v161, v161
	v_rcp_f32_e32 v162, v162
	v_rcp_f32_e32 v163, v163
	v_pk_fma_f32 v[100:101], v[100:101], s[100:101], s[100:101]
	v_pk_fma_f32 v[102:103], v[102:103], s[100:101], s[100:101]
	v_pk_mul_f32 v[96:97], v[96:97], v[160:161]
	v_pk_mul_f32 v[98:99], v[98:99], v[162:163]
	v_pk_mul_f32 v[96:97], v[100:101], v[96:97]
	v_pk_mul_f32 v[98:99], v[102:103], v[98:99]
	v_cvt_pk_fp8_f32 v96, v96, v97
	v_cvt_pk_fp8_f32 v96, v98, v99 op_sel:[0,0,1]
	v_cvt_f32_i32_e32 v80, v80
	v_cvt_f32_i32_e32 v81, v81
	v_cvt_f32_i32_e32 v82, v82
	v_cvt_f32_i32_e32 v83, v83
	v_cvt_f32_i32_e32 v84, v84
	v_cvt_f32_i32_e32 v85, v85
	v_cvt_f32_i32_e32 v86, v86
	v_cvt_f32_i32_e32 v87, v87
	v_pk_mul_f32 v[202:203], v[144:145], v[154:155] op_sel:[0,1] op_sel_hi:[1,1]
	v_pk_mul_f32 v[204:205], v[146:147], v[154:155] op_sel:[0,1] op_sel_hi:[1,1]
	v_pk_fma_f32 v[80:81], v[80:81], v[202:203], v[136:137]
	v_pk_fma_f32 v[82:83], v[82:83], v[204:205], v[138:139]
	v_pk_mul_f32 v[202:203], v[148:149], v[154:155] op_sel:[0,1] op_sel_hi:[1,1]
	v_pk_mul_f32 v[204:205], v[150:151], v[154:155] op_sel:[0,1] op_sel_hi:[1,1]
	v_min_f32_e32 v80, 0x41898193, v80
	v_min_f32_e32 v81, 0x41898193, v81
	v_min_f32_e32 v82, 0x41898193, v82
	v_min_f32_e32 v83, 0x41898193, v83
	v_pk_fma_f32 v[84:85], v[84:85], v[202:203], v[140:141]
	v_pk_fma_f32 v[86:87], v[86:87], v[204:205], v[142:143]
	v_exp_f32_e64 v202, -v80
	v_exp_f32_e64 v203, -v81
	v_exp_f32_e64 v204, -v82
	v_exp_f32_e64 v205, -v83
	v_med3_f32 v84, v84, s8, v199
	v_med3_f32 v85, v85, s8, v199
	v_med3_f32 v86, v86, s8, v199
	v_med3_f32 v87, v87, s8, v199
	v_pk_add_f32 v[202:203], v[202:203], 1.0 op_sel_hi:[1,0]
	v_pk_add_f32 v[204:205], v[204:205], 1.0 op_sel_hi:[1,0]
	v_rcp_f32_e32 v202, v202
	v_rcp_f32_e32 v203, v203
	v_rcp_f32_e32 v204, v204
	v_rcp_f32_e32 v205, v205
	v_pk_fma_f32 v[84:85], v[84:85], s[100:101], s[100:101]
	v_pk_fma_f32 v[86:87], v[86:87], s[100:101], s[100:101]
	v_pk_mul_f32 v[80:81], v[80:81], v[202:203]
	v_pk_mul_f32 v[82:83], v[82:83], v[204:205]
	v_pk_mul_f32 v[80:81], v[84:85], v[80:81]
	v_pk_mul_f32 v[82:83], v[86:87], v[82:83]
	v_cvt_pk_fp8_f32 v98, v80, v81
	v_cvt_pk_fp8_f32 v98, v82, v83 op_sel:[0,0,1]
	v_cvt_f32_i32_e32 v64, v64
	v_cvt_f32_i32_e32 v65, v65
	v_cvt_f32_i32_e32 v66, v66
	v_cvt_f32_i32_e32 v67, v67
	v_cvt_f32_i32_e32 v68, v68
	v_cvt_f32_i32_e32 v69, v69
	v_cvt_f32_i32_e32 v70, v70
	v_cvt_f32_i32_e32 v71, v71
	v_pk_mul_f32 v[160:161], v[144:145], v[156:157] op_sel_hi:[1,0]
	v_pk_mul_f32 v[162:163], v[146:147], v[156:157] op_sel_hi:[1,0]
	v_pk_fma_f32 v[64:65], v[64:65], v[160:161], v[136:137]
	v_pk_fma_f32 v[66:67], v[66:67], v[162:163], v[138:139]
	v_pk_mul_f32 v[160:161], v[148:149], v[156:157] op_sel_hi:[1,0]
	v_pk_mul_f32 v[162:163], v[150:151], v[156:157] op_sel_hi:[1,0]
	v_min_f32_e32 v64, 0x41898193, v64
	v_min_f32_e32 v65, 0x41898193, v65
	v_min_f32_e32 v66, 0x41898193, v66
	v_min_f32_e32 v67, 0x41898193, v67
	v_pk_fma_f32 v[68:69], v[68:69], v[160:161], v[140:141]
	v_pk_fma_f32 v[70:71], v[70:71], v[162:163], v[142:143]
	v_exp_f32_e64 v160, -v64
	v_exp_f32_e64 v161, -v65
	v_exp_f32_e64 v162, -v66
	v_exp_f32_e64 v163, -v67
	v_med3_f32 v68, v68, s8, v199
	v_med3_f32 v69, v69, s8, v199
	v_med3_f32 v70, v70, s8, v199
	v_med3_f32 v71, v71, s8, v199
	v_pk_add_f32 v[160:161], v[160:161], 1.0 op_sel_hi:[1,0]
	v_pk_add_f32 v[162:163], v[162:163], 1.0 op_sel_hi:[1,0]
	v_rcp_f32_e32 v160, v160
	v_rcp_f32_e32 v161, v161
	v_rcp_f32_e32 v162, v162
	v_rcp_f32_e32 v163, v163
	v_pk_fma_f32 v[68:69], v[68:69], s[100:101], s[100:101]
	v_pk_fma_f32 v[70:71], v[70:71], s[100:101], s[100:101]
	v_pk_mul_f32 v[64:65], v[64:65], v[160:161]
	v_pk_mul_f32 v[66:67], v[66:67], v[162:163]
	v_pk_mul_f32 v[64:65], v[68:69], v[64:65]
	v_pk_mul_f32 v[66:67], v[70:71], v[66:67]
	v_cvt_pk_fp8_f32 v64, v64, v65
	v_cvt_pk_fp8_f32 v64, v66, v67 op_sel:[0,0,1]
	v_cvt_f32_i32_e32 v44, v44
	v_cvt_f32_i32_e32 v45, v45
	v_cvt_f32_i32_e32 v46, v46
	v_cvt_f32_i32_e32 v47, v47
	v_cvt_f32_i32_e32 v48, v48
	v_cvt_f32_i32_e32 v49, v49
	v_cvt_f32_i32_e32 v50, v50
	v_cvt_f32_i32_e32 v51, v51
	v_pk_mul_f32 v[202:203], v[144:145], v[156:157] op_sel:[0,1] op_sel_hi:[1,1]
	v_pk_mul_f32 v[204:205], v[146:147], v[156:157] op_sel:[0,1] op_sel_hi:[1,1]
	v_pk_fma_f32 v[44:45], v[44:45], v[202:203], v[136:137]
	v_pk_fma_f32 v[46:47], v[46:47], v[204:205], v[138:139]
	v_pk_mul_f32 v[202:203], v[148:149], v[156:157] op_sel:[0,1] op_sel_hi:[1,1]
	v_pk_mul_f32 v[204:205], v[150:151], v[156:157] op_sel:[0,1] op_sel_hi:[1,1]
	v_min_f32_e32 v44, 0x41898193, v44
	v_min_f32_e32 v45, 0x41898193, v45
; #define PG8_LAS __attribute__((address_space(3)))
;     __device__ __forceinline__ void operator()(const i32x4 (&acc)[2][2][4][2], const Unit& u, int wr, int wc, int fr, int fq, PG8_LAS unsigned* scr) const {
;     ...
;         for (int n = 0; n < 2; ++n) { bgv[n] = *(const PG8_LAS f32x4*)(scr + 512 + cl + 4 * n) * C2; buv[n] = *(const PG8_LAS f32x4*)(scr + 512 + 128 + cl + 4 * n);
;             csg[n] = *(const PG8_LAS f32x4*)(scr + 256 + cl + 4 * n) * (C2 / 127.0f); csu[n] = *(const PG8_LAS f32x4*)(scr + 256 + 128 + cl + 4 * n) * (1.0f / 127.0f); }
; #pragma unroll
;         for (int ai = 0; ai < 2; ++ai)
; #pragma unroll
;             for (int mp = 0; mp < 4; mp += 2) { unsigned wp[2][2];
; #pragma unroll
;                 for (int hm = 0; hm < 2; ++hm) { const int m = mp + hm; const int r = ai * HALF + wr * 64 + m * 16 + fr; const float rs = __uint_as_float(scr[r]); float o[8];
; #pragma unroll
;                     for (int n = 0; n < 2; ++n) { const f32x4 sgr = csg[n] * rs, sur = csu[n] * rs;
; #pragma unroll
;                         for (int q = 0; q < 4; ++q) { const float h = fminf(__builtin_fmaf((float)acc[ai][0][m][n][q], sgr[q], bgv[n][q]), 7.0f * C2), up = fminf(fmaxf(__builtin_fmaf((float)acc[ai][1][m][n][q], sur[q], buv[n][q]), -7.0f), 7.0f);
;                             const float sg = __builtin_amdgcn_rcpf(1.0f + __builtin_amdgcn_exp2f(-h)); o[4 * n + q] = __builtin_fmaf(up, ACT_SC / C2, ACT_SC / C2) * (h * sg); } }
;                     int w0 = __builtin_amdgcn_cvt_pk_fp8_f32(o[0], o[1], 0, false); w0 = __builtin_amdgcn_cvt_pk_fp8_f32(o[2], o[3], w0, true);
;                     int w1 = __builtin_amdgcn_cvt_pk_fp8_f32(o[4], o[5], 0, false); w1 = __builtin_amdgcn_cvt_pk_fp8_f32(o[6], o[7], w1, true);
;                     wp[hm][0] = (unsigned)w0; wp[hm][1] = (unsigned)w1; }
	v_min_f32_e32 v46, 0x41898193, v46
	v_min_f32_e32 v47, 0x41898193, v47
	v_pk_fma_f32 v[48:49], v[48:49], v[202:203], v[140:141]
	v_pk_fma_f32 v[50:51], v[50:51], v[204:205], v[142:143]
	v_exp_f32_e64 v202, -v44
	v_exp_f32_e64 v203, -v45
	v_exp_f32_e64 v204, -v46
	v_exp_f32_e64 v205, -v47
	v_med3_f32 v48, v48, s8, v199
	v_med3_f32 v49, v49, s8, v199
	v_med3_f32 v50, v50, s8, v199
	v_med3_f32 v51, v51, s8, v199
	v_pk_add_f32 v[202:203], v[202:203], 1.0 op_sel_hi:[1,0]
	v_pk_add_f32 v[204:205], v[204:205], 1.0 op_sel_hi:[1,0]
	v_rcp_f32_e32 v202, v202
	v_rcp_f32_e32 v203, v203
	v_rcp_f32_e32 v204, v204
	v_rcp_f32_e32 v205, v205
	v_pk_fma_f32 v[48:49], v[48:49], s[100:101], s[100:101]
	v_pk_fma_f32 v[50:51], v[50:51], s[100:101], s[100:101]
	v_pk_mul_f32 v[44:45], v[44:45], v[202:203]
	v_pk_mul_f32 v[46:47], v[46:47], v[204:205]
	v_pk_mul_f32 v[44:45], v[48:49], v[44:45]
	v_pk_mul_f32 v[46:47], v[50:51], v[46:47]
	v_cvt_pk_fp8_f32 v66, v44, v45
	v_cvt_pk_fp8_f32 v66, v46, v47 op_sel:[0,0,1]
	v_cvt_f32_i32_e32 v24, v24
	v_cvt_f32_i32_e32 v25, v25
	v_cvt_f32_i32_e32 v26, v26
	v_cvt_f32_i32_e32 v27, v27
	v_cvt_f32_i32_e32 v28, v28
	v_cvt_f32_i32_e32 v29, v29
	v_cvt_f32_i32_e32 v30, v30
	v_cvt_f32_i32_e32 v31, v31
	v_pk_mul_f32 v[160:161], v[144:145], v[158:159] op_sel_hi:[1,0]
	v_pk_mul_f32 v[162:163], v[146:147], v[158:159] op_sel_hi:[1,0]
	v_pk_fma_f32 v[24:25], v[24:25], v[160:161], v[136:137]
	v_pk_fma_f32 v[26:27], v[26:27], v[162:163], v[138:139]
	v_pk_mul_f32 v[160:161], v[148:149], v[158:159] op_sel_hi:[1,0]
	v_pk_mul_f32 v[162:163], v[150:151], v[158:159] op_sel_hi:[1,0]
	v_min_f32_e32 v24, 0x41898193, v24
	v_min_f32_e32 v25, 0x41898193, v25
	v_min_f32_e32 v26, 0x41898193, v26
	v_min_f32_e32 v27, 0x41898193, v27
	v_pk_fma_f32 v[28:29], v[28:29], v[160:161], v[140:141]
	v_pk_fma_f32 v[30:31], v[30:31], v[162:163], v[142:143]
	v_exp_f32_e64 v160, -v24
	v_exp_f32_e64 v161, -v25
	v_exp_f32_e64 v162, -v26
	v_exp_f32_e64 v163, -v27
	v_med3_f32 v28, v28, s8, v199
	v_med3_f32 v29, v29, s8, v199
	v_med3_f32 v30, v30, s8, v199
	v_med3_f32 v31, v31, s8, v199
	v_pk_add_f32 v[160:161], v[160:161], 1.0 op_sel_hi:[1,0]
	v_pk_add_f32 v[162:163], v[162:163], 1.0 op_sel_hi:[1,0]
	v_rcp_f32_e32 v160, v160
	v_rcp_f32_e32 v161, v161
	v_rcp_f32_e32 v162, v162
	v_rcp_f32_e32 v163, v163
	v_pk_fma_f32 v[28:29], v[28:29], s[100:101], s[100:101]
	v_pk_fma_f32 v[30:31], v[30:31], s[100:101], s[100:101]
	v_pk_mul_f32 v[24:25], v[24:25], v[160:161]
	v_pk_mul_f32 v[26:27], v[26:27], v[162:163]
	v_pk_mul_f32 v[24:25], v[28:29], v[24:25]
	v_pk_mul_f32 v[26:27], v[30:31], v[26:27]
	v_cvt_pk_fp8_f32 v24, v24, v25
	v_cvt_pk_fp8_f32 v24, v26, v27 op_sel:[0,0,1]
	v_cvt_f32_i32_e32 v8, v8
	v_cvt_f32_i32_e32 v9, v9
	v_cvt_f32_i32_e32 v10, v10
	v_cvt_f32_i32_e32 v11, v11
	v_cvt_f32_i32_e32 v12, v12
	v_cvt_f32_i32_e32 v13, v13
	v_cvt_f32_i32_e32 v14, v14
	v_cvt_f32_i32_e32 v15, v15
	v_pk_mul_f32 v[202:203], v[144:145], v[158:159] op_sel:[0,1] op_sel_hi:[1,1]
	v_pk_mul_f32 v[204:205], v[146:147], v[158:159] op_sel:[0,1] op_sel_hi:[1,1]
	v_pk_fma_f32 v[8:9], v[8:9], v[202:203], v[136:137]
	v_pk_fma_f32 v[10:11], v[10:11], v[204:205], v[138:139]
	v_pk_mul_f32 v[202:203], v[148:149], v[158:159] op_sel:[0,1] op_sel_hi:[1,1]
	v_pk_mul_f32 v[204:205], v[150:151], v[158:159] op_sel:[0,1] op_sel_hi:[1,1]
	v_min_f32_e32 v8, 0x41898193, v8
	v_min_f32_e32 v9, 0x41898193, v9
	v_min_f32_e32 v10, 0x41898193, v10
	v_min_f32_e32 v11, 0x41898193, v11
	v_pk_fma_f32 v[12:13], v[12:13], v[202:203], v[140:141]
	v_pk_fma_f32 v[14:15], v[14:15], v[204:205], v[142:143]
	v_exp_f32_e64 v202, -v8
	v_exp_f32_e64 v203, -v9
	v_exp_f32_e64 v204, -v10
	v_exp_f32_e64 v205, -v11
	v_med3_f32 v12, v12, s8, v199
	v_med3_f32 v13, v13, s8, v199
	v_med3_f32 v14, v14, s8, v199
	v_med3_f32 v15, v15, s8, v199
	v_pk_add_f32 v[202:203], v[202:203], 1.0 op_sel_hi:[1,0]
	v_pk_add_f32 v[204:205], v[204:205], 1.0 op_sel_hi:[1,0]
	v_rcp_f32_e32 v202, v202
	v_rcp_f32_e32 v203, v203
	v_rcp_f32_e32 v204, v204
	v_rcp_f32_e32 v205, v205
	v_pk_fma_f32 v[12:13], v[12:13], s[100:101], s[100:101]
	v_pk_fma_f32 v[14:15], v[14:15], s[100:101], s[100:101]
	v_pk_mul_f32 v[8:9], v[8:9], v[202:203]
	v_pk_mul_f32 v[10:11], v[10:11], v[204:205]
	v_pk_mul_f32 v[8:9], v[12:13], v[8:9]
	v_pk_mul_f32 v[10:11], v[14:15], v[10:11]
	v_cvt_pk_fp8_f32 v26, v8, v9
	v_cvt_pk_fp8_f32 v26, v10, v11 op_sel:[0,0,1]
	v_add_u32_e32 v160, 0x21110, v208
	ds_read_b128 v[136:139], v160
	v_add_u32_e32 v160, 0x21310, v208
	ds_read_b128 v[140:143], v160
	v_add_u32_e32 v160, 0x20d10, v208
	ds_read_b128 v[144:147], v160
	v_add_u32_e32 v160, 0x20f10, v208
	ds_read_b128 v[148:151], v160
	s_waitcnt lgkmcnt(0)
; #define GAS __attribute__((address_space(1)))
;     __device__ __forceinline__ void operator()(const i32x4 (&acc)[2][2][4][2], const Unit& u, int wr, int wc, int fr, int fq, PG8_LAS unsigned* scr) const {
;     ...
;                 for (int hm = 0; hm < 2; ++hm) { const int m = mp + hm; const int r = ai * HALF + wr * 64 + m * 16 + fr; const float rs = __uint_as_float(scr[r]); float o[8];
; #pragma unroll
;                     for (int n = 0; n < 2; ++n) { const f32x4 sgr = csg[n] * rs, sur = csu[n] * rs;
; #pragma unroll
;                         for (int q = 0; q < 4; ++q) { const float h = fminf(__builtin_fmaf((float)acc[ai][0][m][n][q], sgr[q], bgv[n][q]), 7.0f * C2), up = fminf(fmaxf(__builtin_fmaf((float)acc[ai][1][m][n][q], sur[q], buv[n][q]), -7.0f), 7.0f);
;                             const float sg = __builtin_amdgcn_rcpf(1.0f + __builtin_amdgcn_exp2f(-h)); o[4 * n + q] = __builtin_fmaf(up, ACT_SC / C2, ACT_SC / C2) * (h * sg); } }
;                     int w0 = __builtin_amdgcn_cvt_pk_fp8_f32(o[0], o[1], 0, false); w0 = __builtin_amdgcn_cvt_pk_fp8_f32(o[2], o[3], w0, true);
;                     int w1 = __builtin_amdgcn_cvt_pk_fp8_f32(o[4], o[5], 0, false); w1 = __builtin_amdgcn_cvt_pk_fp8_f32(o[6], o[7], w1, true);
;                     wp[hm][0] = (unsigned)w0; wp[hm][1] = (unsigned)w1; }
;                 { auto r0 = __builtin_amdgcn_permlane16_swap(wp[0][0], wp[1][0], false, false); wp[0][0] = r0[0]; wp[1][0] = r0[1];
;                   auto r1 = __builtin_amdgcn_permlane16_swap(wp[0][1], wp[1][1], false, false); wp[0][1] = r1[0]; wp[1][1] = r1[1]; }
;                 const int odd = fq & 1;
;                 const size_t arow = (size_t)(row0 + ai * HALF + (mp + odd) * 16);
;                 *(GAS u32x4*)(act + arow * 1024 + (c0 - 8 * odd)) = (u32x4){wp[0][0], wp[0][1], wp[1][0], wp[1][1]};
	v_mul_f32_e32 v136, 0x401d265f, v136
	v_mul_f32_e32 v137, 0x401d265f, v137
	v_mul_f32_e32 v138, 0x401d265f, v138
	v_mul_f32_e32 v139, 0x401d265f, v139
	v_mul_f32_e32 v144, 0x3c9e6325, v144
	v_mul_f32_e32 v145, 0x3c9e6325, v145
	v_mul_f32_e32 v146, 0x3c9e6325, v146
	v_mul_f32_e32 v147, 0x3c9e6325, v147
	v_mul_f32_e32 v148, 0x3c010204, v148
	v_mul_f32_e32 v149, 0x3c010204, v149
	v_mul_f32_e32 v150, 0x3c010204, v150
	v_mul_f32_e32 v151, 0x3c010204, v151
	v_cvt_f32_i32_e32 v120, v120
	v_cvt_f32_i32_e32 v121, v121
	v_cvt_f32_i32_e32 v122, v122
	v_cvt_f32_i32_e32 v123, v123
	v_cvt_f32_i32_e32 v124, v124
	v_cvt_f32_i32_e32 v125, v125
	v_cvt_f32_i32_e32 v126, v126
	v_cvt_f32_i32_e32 v127, v127
	v_pk_mul_f32 v[160:161], v[144:145], v[152:153] op_sel_hi:[1,0]
	v_pk_mul_f32 v[162:163], v[146:147], v[152:153] op_sel_hi:[1,0]
	v_pk_fma_f32 v[120:121], v[120:121], v[160:161], v[136:137]
	v_pk_fma_f32 v[122:123], v[122:123], v[162:163], v[138:139]
	v_pk_mul_f32 v[160:161], v[148:149], v[152:153] op_sel_hi:[1,0]
	v_pk_mul_f32 v[162:163], v[150:151], v[152:153] op_sel_hi:[1,0]
	v_min_f32_e32 v120, 0x41898193, v120
	v_min_f32_e32 v121, 0x41898193, v121
	v_min_f32_e32 v122, 0x41898193, v122
	v_min_f32_e32 v123, 0x41898193, v123
	v_pk_fma_f32 v[124:125], v[124:125], v[160:161], v[140:141]
	v_pk_fma_f32 v[126:127], v[126:127], v[162:163], v[142:143]
	v_exp_f32_e64 v160, -v120
	v_exp_f32_e64 v161, -v121
	v_exp_f32_e64 v162, -v122
	v_exp_f32_e64 v163, -v123
	v_med3_f32 v124, v124, s8, v199
	v_med3_f32 v125, v125, s8, v199
	v_med3_f32 v126, v126, s8, v199
	v_med3_f32 v127, v127, s8, v199
	v_pk_add_f32 v[160:161], v[160:161], 1.0 op_sel_hi:[1,0]
	v_pk_add_f32 v[162:163], v[162:163], 1.0 op_sel_hi:[1,0]
	v_rcp_f32_e32 v160, v160
	v_rcp_f32_e32 v161, v161
	v_rcp_f32_e32 v162, v162
	v_rcp_f32_e32 v163, v163
	v_pk_fma_f32 v[124:125], v[124:125], s[100:101], s[100:101]
	v_pk_fma_f32 v[126:127], v[126:127], s[100:101], s[100:101]
	v_pk_mul_f32 v[120:121], v[120:121], v[160:161]
	v_pk_mul_f32 v[122:123], v[122:123], v[162:163]
	v_pk_mul_f32 v[120:121], v[124:125], v[120:121]
	v_pk_mul_f32 v[122:123], v[126:127], v[122:123]
	v_cvt_pk_fp8_f32 v129, v120, v121
	v_cvt_pk_fp8_f32 v129, v122, v123 op_sel:[0,0,1]
	v_cvt_f32_i32_e32 v104, v104
	v_cvt_f32_i32_e32 v105, v105
	v_cvt_f32_i32_e32 v106, v106
	v_cvt_f32_i32_e32 v107, v107
	v_cvt_f32_i32_e32 v108, v108
	v_cvt_f32_i32_e32 v109, v109
	v_cvt_f32_i32_e32 v110, v110
	v_cvt_f32_i32_e32 v111, v111
	v_pk_mul_f32 v[202:203], v[144:145], v[152:153] op_sel:[0,1] op_sel_hi:[1,1]
	v_pk_mul_f32 v[204:205], v[146:147], v[152:153] op_sel:[0,1] op_sel_hi:[1,1]
	v_pk_fma_f32 v[104:105], v[104:105], v[202:203], v[136:137]
	v_pk_fma_f32 v[106:107], v[106:107], v[204:205], v[138:139]
	v_pk_mul_f32 v[202:203], v[148:149], v[152:153] op_sel:[0,1] op_sel_hi:[1,1]
	v_pk_mul_f32 v[204:205], v[150:151], v[152:153] op_sel:[0,1] op_sel_hi:[1,1]
	v_min_f32_e32 v104, 0x41898193, v104
	v_min_f32_e32 v105, 0x41898193, v105
	v_min_f32_e32 v106, 0x41898193, v106
	v_min_f32_e32 v107, 0x41898193, v107
	v_pk_fma_f32 v[108:109], v[108:109], v[202:203], v[140:141]
	v_pk_fma_f32 v[110:111], v[110:111], v[204:205], v[142:143]
	v_exp_f32_e64 v202, -v104
	v_exp_f32_e64 v203, -v105
	v_exp_f32_e64 v204, -v106
	v_exp_f32_e64 v205, -v107
	v_med3_f32 v108, v108, s8, v199
	v_med3_f32 v109, v109, s8, v199
	v_med3_f32 v110, v110, s8, v199
	v_med3_f32 v111, v111, s8, v199
	v_pk_add_f32 v[202:203], v[202:203], 1.0 op_sel_hi:[1,0]
	v_pk_add_f32 v[204:205], v[204:205], 1.0 op_sel_hi:[1,0]
	v_rcp_f32_e32 v202, v202
	v_rcp_f32_e32 v203, v203
	v_rcp_f32_e32 v204, v204
	v_rcp_f32_e32 v205, v205
	v_pk_fma_f32 v[108:109], v[108:109], s[100:101], s[100:101]
	v_pk_fma_f32 v[110:111], v[110:111], s[100:101], s[100:101]
	v_pk_mul_f32 v[104:105], v[104:105], v[202:203]
	v_pk_mul_f32 v[106:107], v[106:107], v[204:205]
	v_pk_mul_f32 v[104:105], v[108:109], v[104:105]
	v_pk_mul_f32 v[106:107], v[110:111], v[106:107]
	v_cvt_pk_fp8_f32 v131, v104, v105
	v_cvt_pk_fp8_f32 v131, v106, v107 op_sel:[0,0,1]
	s_nop 1
	v_permlane16_swap_b32_e32 v128, v130
	v_permlane16_swap_b32_e32 v129, v131
	global_store_dwordx4 v207, v[128:131], s[60:61]
	v_cvt_f32_i32_e32 v88, v88
	v_cvt_f32_i32_e32 v89, v89
	v_cvt_f32_i32_e32 v90, v90
	v_cvt_f32_i32_e32 v91, v91
	v_cvt_f32_i32_e32 v92, v92
	v_cvt_f32_i32_e32 v93, v93
	v_cvt_f32_i32_e32 v94, v94
	v_cvt_f32_i32_e32 v95, v95
	v_pk_mul_f32 v[160:161], v[144:145], v[154:155] op_sel_hi:[1,0]
	v_pk_mul_f32 v[162:163], v[146:147], v[154:155] op_sel_hi:[1,0]
	v_pk_fma_f32 v[88:89], v[88:89], v[160:161], v[136:137]
	v_pk_fma_f32 v[90:91], v[90:91], v[162:163], v[138:139]
	v_pk_mul_f32 v[160:161], v[148:149], v[154:155] op_sel_hi:[1,0]
	v_pk_mul_f32 v[162:163], v[150:151], v[154:155] op_sel_hi:[1,0]
	v_min_f32_e32 v88, 0x41898193, v88
	v_min_f32_e32 v89, 0x41898193, v89
	v_min_f32_e32 v90, 0x41898193, v90
	v_min_f32_e32 v91, 0x41898193, v91
	v_pk_fma_f32 v[92:93], v[92:93], v[160:161], v[140:141]
	v_pk_fma_f32 v[94:95], v[94:95], v[162:163], v[142:143]
	v_exp_f32_e64 v160, -v88
	v_exp_f32_e64 v161, -v89
	v_exp_f32_e64 v162, -v90
	v_exp_f32_e64 v163, -v91
	v_med3_f32 v92, v92, s8, v199
	v_med3_f32 v93, v93, s8, v199
	v_med3_f32 v94, v94, s8, v199
	v_med3_f32 v95, v95, s8, v199
	v_pk_add_f32 v[160:161], v[160:161], 1.0 op_sel_hi:[1,0]
	v_pk_add_f32 v[162:163], v[162:163], 1.0 op_sel_hi:[1,0]
	v_rcp_f32_e32 v160, v160
	v_rcp_f32_e32 v161, v161
	v_rcp_f32_e32 v162, v162
	v_rcp_f32_e32 v163, v163
	v_pk_fma_f32 v[92:93], v[92:93], s[100:101], s[100:101]
	v_pk_fma_f32 v[94:95], v[94:95], s[100:101], s[100:101]
	v_pk_mul_f32 v[88:89], v[88:89], v[160:161]
; #define GAS __attribute__((address_space(1)))
;     __device__ __forceinline__ void operator()(const i32x4 (&acc)[2][2][4][2], const Unit& u, int wr, int wc, int fr, int fq, PG8_LAS unsigned* scr) const {
;     ...
;                 for (int hm = 0; hm < 2; ++hm) { const int m = mp + hm; const int r = ai * HALF + wr * 64 + m * 16 + fr; const float rs = __uint_as_float(scr[r]); float o[8];
; #pragma unroll
;                     for (int n = 0; n < 2; ++n) { const f32x4 sgr = csg[n] * rs, sur = csu[n] * rs;
; #pragma unroll
;                         for (int q = 0; q < 4; ++q) { const float h = fminf(__builtin_fmaf((float)acc[ai][0][m][n][q], sgr[q], bgv[n][q]), 7.0f * C2), up = fminf(fmaxf(__builtin_fmaf((float)acc[ai][1][m][n][q], sur[q], buv[n][q]), -7.0f), 7.0f);
;                             const float sg = __builtin_amdgcn_rcpf(1.0f + __builtin_amdgcn_exp2f(-h)); o[4 * n + q] = __builtin_fmaf(up, ACT_SC / C2, ACT_SC / C2) * (h * sg); } }
;                     int w0 = __builtin_amdgcn_cvt_pk_fp8_f32(o[0], o[1], 0, false); w0 = __builtin_amdgcn_cvt_pk_fp8_f32(o[2], o[3], w0, true);
;                     int w1 = __builtin_amdgcn_cvt_pk_fp8_f32(o[4], o[5], 0, false); w1 = __builtin_amdgcn_cvt_pk_fp8_f32(o[6], o[7], w1, true);
;                     wp[hm][0] = (unsigned)w0; wp[hm][1] = (unsigned)w1; }
;                 { auto r0 = __builtin_amdgcn_permlane16_swap(wp[0][0], wp[1][0], false, false); wp[0][0] = r0[0]; wp[1][0] = r0[1];
;                   auto r1 = __builtin_amdgcn_permlane16_swap(wp[0][1], wp[1][1], false, false); wp[0][1] = r1[0]; wp[1][1] = r1[1]; }
;                 const int odd = fq & 1;
;                 const size_t arow = (size_t)(row0 + ai * HALF + (mp + odd) * 16);
;                 *(GAS u32x4*)(act + arow * 1024 + (c0 - 8 * odd)) = (u32x4){wp[0][0], wp[0][1], wp[1][0], wp[1][1]};
	v_pk_mul_f32 v[90:91], v[90:91], v[162:163]
	v_pk_mul_f32 v[88:89], v[92:93], v[88:89]
	v_pk_mul_f32 v[90:91], v[94:95], v[90:91]
	v_cvt_pk_fp8_f32 v97, v88, v89
	v_cvt_pk_fp8_f32 v97, v90, v91 op_sel:[0,0,1]
	v_cvt_f32_i32_e32 v72, v72
	v_cvt_f32_i32_e32 v73, v73
	v_cvt_f32_i32_e32 v74, v74
	v_cvt_f32_i32_e32 v75, v75
	v_cvt_f32_i32_e32 v76, v76
	v_cvt_f32_i32_e32 v77, v77
	v_cvt_f32_i32_e32 v78, v78
	v_cvt_f32_i32_e32 v79, v79
	v_pk_mul_f32 v[202:203], v[144:145], v[154:155] op_sel:[0,1] op_sel_hi:[1,1]
	v_pk_mul_f32 v[204:205], v[146:147], v[154:155] op_sel:[0,1] op_sel_hi:[1,1]
	v_pk_fma_f32 v[72:73], v[72:73], v[202:203], v[136:137]
	v_pk_fma_f32 v[74:75], v[74:75], v[204:205], v[138:139]
	v_pk_mul_f32 v[202:203], v[148:149], v[154:155] op_sel:[0,1] op_sel_hi:[1,1]
	v_pk_mul_f32 v[204:205], v[150:151], v[154:155] op_sel:[0,1] op_sel_hi:[1,1]
	v_min_f32_e32 v72, 0x41898193, v72
	v_min_f32_e32 v73, 0x41898193, v73
	v_min_f32_e32 v74, 0x41898193, v74
	v_min_f32_e32 v75, 0x41898193, v75
	v_pk_fma_f32 v[76:77], v[76:77], v[202:203], v[140:141]
	v_pk_fma_f32 v[78:79], v[78:79], v[204:205], v[142:143]
	v_exp_f32_e64 v202, -v72
	v_exp_f32_e64 v203, -v73
	v_exp_f32_e64 v204, -v74
	v_exp_f32_e64 v205, -v75
	v_med3_f32 v76, v76, s8, v199
	v_med3_f32 v77, v77, s8, v199
	v_med3_f32 v78, v78, s8, v199
	v_med3_f32 v79, v79, s8, v199
	v_pk_add_f32 v[202:203], v[202:203], 1.0 op_sel_hi:[1,0]
	v_pk_add_f32 v[204:205], v[204:205], 1.0 op_sel_hi:[1,0]
	v_rcp_f32_e32 v202, v202
	v_rcp_f32_e32 v203, v203
	v_rcp_f32_e32 v204, v204
	v_rcp_f32_e32 v205, v205
	v_pk_fma_f32 v[76:77], v[76:77], s[100:101], s[100:101]
	v_pk_fma_f32 v[78:79], v[78:79], s[100:101], s[100:101]
	v_pk_mul_f32 v[72:73], v[72:73], v[202:203]
	v_pk_mul_f32 v[74:75], v[74:75], v[204:205]
	v_pk_mul_f32 v[72:73], v[76:77], v[72:73]
	v_pk_mul_f32 v[74:75], v[78:79], v[74:75]
	v_cvt_pk_fp8_f32 v99, v72, v73
	v_cvt_pk_fp8_f32 v99, v74, v75 op_sel:[0,0,1]
	s_nop 1
	v_permlane16_swap_b32_e32 v96, v98
	v_permlane16_swap_b32_e32 v97, v99
	v_add_u32_e32 v160, 0x8000, v207
	global_store_dwordx4 v160, v[96:99], s[60:61]
	v_cvt_f32_i32_e32 v56, v56
	v_cvt_f32_i32_e32 v57, v57
	v_cvt_f32_i32_e32 v58, v58
	v_cvt_f32_i32_e32 v59, v59
	v_cvt_f32_i32_e32 v60, v60
	v_cvt_f32_i32_e32 v61, v61
	v_cvt_f32_i32_e32 v62, v62
	v_cvt_f32_i32_e32 v63, v63
	v_pk_mul_f32 v[160:161], v[144:145], v[156:157] op_sel_hi:[1,0]
	v_pk_mul_f32 v[162:163], v[146:147], v[156:157] op_sel_hi:[1,0]
	v_pk_fma_f32 v[56:57], v[56:57], v[160:161], v[136:137]
	v_pk_fma_f32 v[58:59], v[58:59], v[162:163], v[138:139]
	v_pk_mul_f32 v[160:161], v[148:149], v[156:157] op_sel_hi:[1,0]
	v_pk_mul_f32 v[162:163], v[150:151], v[156:157] op_sel_hi:[1,0]
	v_min_f32_e32 v56, 0x41898193, v56
	v_min_f32_e32 v57, 0x41898193, v57
	v_min_f32_e32 v58, 0x41898193, v58
	v_min_f32_e32 v59, 0x41898193, v59
	v_pk_fma_f32 v[60:61], v[60:61], v[160:161], v[140:141]
	v_pk_fma_f32 v[62:63], v[62:63], v[162:163], v[142:143]
	v_exp_f32_e64 v160, -v56
	v_exp_f32_e64 v161, -v57
	v_exp_f32_e64 v162, -v58
	v_exp_f32_e64 v163, -v59
	v_med3_f32 v60, v60, s8, v199
	v_med3_f32 v61, v61, s8, v199
	v_med3_f32 v62, v62, s8, v199
	v_med3_f32 v63, v63, s8, v199
	v_pk_add_f32 v[160:161], v[160:161], 1.0 op_sel_hi:[1,0]
	v_pk_add_f32 v[162:163], v[162:163], 1.0 op_sel_hi:[1,0]
	v_rcp_f32_e32 v160, v160
	v_rcp_f32_e32 v161, v161
	v_rcp_f32_e32 v162, v162
	v_rcp_f32_e32 v163, v163
	v_pk_fma_f32 v[60:61], v[60:61], s[100:101], s[100:101]
	v_pk_fma_f32 v[62:63], v[62:63], s[100:101], s[100:101]
	v_pk_mul_f32 v[56:57], v[56:57], v[160:161]
	v_pk_mul_f32 v[58:59], v[58:59], v[162:163]
	v_pk_mul_f32 v[56:57], v[60:61], v[56:57]
	v_pk_mul_f32 v[58:59], v[62:63], v[58:59]
	v_cvt_pk_fp8_f32 v65, v56, v57
	v_cvt_pk_fp8_f32 v65, v58, v59 op_sel:[0,0,1]
	v_cvt_f32_i32_e32 v32, v32
	v_cvt_f32_i32_e32 v33, v33
	v_cvt_f32_i32_e32 v34, v34
	v_cvt_f32_i32_e32 v35, v35
	v_cvt_f32_i32_e32 v36, v36
	v_cvt_f32_i32_e32 v37, v37
	v_cvt_f32_i32_e32 v38, v38
	v_cvt_f32_i32_e32 v39, v39
	v_pk_mul_f32 v[202:203], v[144:145], v[156:157] op_sel:[0,1] op_sel_hi:[1,1]
	v_pk_mul_f32 v[204:205], v[146:147], v[156:157] op_sel:[0,1] op_sel_hi:[1,1]
	v_pk_fma_f32 v[32:33], v[32:33], v[202:203], v[136:137]
	v_pk_fma_f32 v[34:35], v[34:35], v[204:205], v[138:139]
	v_pk_mul_f32 v[202:203], v[148:149], v[156:157] op_sel:[0,1] op_sel_hi:[1,1]
	v_pk_mul_f32 v[204:205], v[150:151], v[156:157] op_sel:[0,1] op_sel_hi:[1,1]
	v_min_f32_e32 v32, 0x41898193, v32
	v_min_f32_e32 v33, 0x41898193, v33
	v_min_f32_e32 v34, 0x41898193, v34
	v_min_f32_e32 v35, 0x41898193, v35
	v_pk_fma_f32 v[36:37], v[36:37], v[202:203], v[140:141]
	v_pk_fma_f32 v[38:39], v[38:39], v[204:205], v[142:143]
	v_exp_f32_e64 v202, -v32
	v_exp_f32_e64 v203, -v33
	v_exp_f32_e64 v204, -v34
	v_exp_f32_e64 v205, -v35
	v_med3_f32 v36, v36, s8, v199
	v_med3_f32 v37, v37, s8, v199
; #define GAS __attribute__((address_space(1)))
; #define PG8_BAR __builtin_amdgcn_s_barrier()
;     __device__ __forceinline__ void operator()(const i32x4 (&acc)[2][2][4][2], const Unit& u, int wr, int wc, int fr, int fq, PG8_LAS unsigned* scr) const {
;     ...
;                 for (int hm = 0; hm < 2; ++hm) { const int m = mp + hm; const int r = ai * HALF + wr * 64 + m * 16 + fr; const float rs = __uint_as_float(scr[r]); float o[8];
; #pragma unroll
;                     for (int n = 0; n < 2; ++n) { const f32x4 sgr = csg[n] * rs, sur = csu[n] * rs;
; #pragma unroll
;                         for (int q = 0; q < 4; ++q) { const float h = fminf(__builtin_fmaf((float)acc[ai][0][m][n][q], sgr[q], bgv[n][q]), 7.0f * C2), up = fminf(fmaxf(__builtin_fmaf((float)acc[ai][1][m][n][q], sur[q], buv[n][q]), -7.0f), 7.0f);
;                             const float sg = __builtin_amdgcn_rcpf(1.0f + __builtin_amdgcn_exp2f(-h)); o[4 * n + q] = __builtin_fmaf(up, ACT_SC / C2, ACT_SC / C2) * (h * sg); } }
;                     int w0 = __builtin_amdgcn_cvt_pk_fp8_f32(o[0], o[1], 0, false); w0 = __builtin_amdgcn_cvt_pk_fp8_f32(o[2], o[3], w0, true);
;                     int w1 = __builtin_amdgcn_cvt_pk_fp8_f32(o[4], o[5], 0, false); w1 = __builtin_amdgcn_cvt_pk_fp8_f32(o[6], o[7], w1, true);
;                     wp[hm][0] = (unsigned)w0; wp[hm][1] = (unsigned)w1; }
;                 { auto r0 = __builtin_amdgcn_permlane16_swap(wp[0][0], wp[1][0], false, false); wp[0][0] = r0[0]; wp[1][0] = r0[1];
;                   auto r1 = __builtin_amdgcn_permlane16_swap(wp[0][1], wp[1][1], false, false); wp[0][1] = r1[0]; wp[1][1] = r1[1]; }
;                 const int odd = fq & 1;
;                 const size_t arow = (size_t)(row0 + ai * HALF + (mp + odd) * 16);
;                 *(GAS u32x4*)(act + arow * 1024 + (c0 - 8 * odd)) = (u32x4){wp[0][0], wp[0][1], wp[1][0], wp[1][1]};
;                 __builtin_amdgcn_sched_barrier(0); }
; template <class Epi, class Sched, bool GATHER, int MODE>
; __device__ __forceinline__ void gemm_phase(PG8_LAS unsigned char* lds, PG8_LAS unsigned* scr, const Gemm g, const Sched& S, const Epi& E, int tid_in) {
;     ...
;         if (!has_next) break;
;         cur = nxt; cA = nA; cB = nB; ++ui;
;         if (GATHER) { const u32x4 nx = gather_read(cur); c0[0] = nx[0]; c0[1] = nx[1]; c1[0] = nx[2]; c1[1] = nx[3]; }
;         if (wr == 1) PG8_BAR;
	v_med3_f32 v38, v38, s8, v199
	v_med3_f32 v39, v39, s8, v199
	v_pk_add_f32 v[202:203], v[202:203], 1.0 op_sel_hi:[1,0]
	v_pk_add_f32 v[204:205], v[204:205], 1.0 op_sel_hi:[1,0]
	v_rcp_f32_e32 v202, v202
	v_rcp_f32_e32 v203, v203
	v_rcp_f32_e32 v204, v204
	v_rcp_f32_e32 v205, v205
	v_pk_fma_f32 v[36:37], v[36:37], s[100:101], s[100:101]
	v_pk_fma_f32 v[38:39], v[38:39], s[100:101], s[100:101]
	v_pk_mul_f32 v[32:33], v[32:33], v[202:203]
	v_pk_mul_f32 v[34:35], v[34:35], v[204:205]
	v_pk_mul_f32 v[32:33], v[36:37], v[32:33]
	v_pk_mul_f32 v[34:35], v[38:39], v[34:35]
	v_cvt_pk_fp8_f32 v67, v32, v33
	v_cvt_pk_fp8_f32 v67, v34, v35 op_sel:[0,0,1]
	s_nop 1
	v_permlane16_swap_b32_e32 v64, v66
	v_permlane16_swap_b32_e32 v65, v67
	v_add_u32_e32 v160, 0x20000, v207
	global_store_dwordx4 v160, v[64:67], s[60:61]
	v_cvt_f32_i32_e32 v16, v16
	v_cvt_f32_i32_e32 v17, v17
	v_cvt_f32_i32_e32 v18, v18
	v_cvt_f32_i32_e32 v19, v19
	v_cvt_f32_i32_e32 v20, v20
	v_cvt_f32_i32_e32 v21, v21
	v_cvt_f32_i32_e32 v22, v22
	v_cvt_f32_i32_e32 v23, v23
	v_pk_mul_f32 v[160:161], v[144:145], v[158:159] op_sel_hi:[1,0]
	v_pk_mul_f32 v[162:163], v[146:147], v[158:159] op_sel_hi:[1,0]
	v_pk_fma_f32 v[16:17], v[16:17], v[160:161], v[136:137]
	v_pk_fma_f32 v[18:19], v[18:19], v[162:163], v[138:139]
	v_pk_mul_f32 v[160:161], v[148:149], v[158:159] op_sel_hi:[1,0]
	v_pk_mul_f32 v[162:163], v[150:151], v[158:159] op_sel_hi:[1,0]
	v_min_f32_e32 v16, 0x41898193, v16
	v_min_f32_e32 v17, 0x41898193, v17
	v_min_f32_e32 v18, 0x41898193, v18
	v_min_f32_e32 v19, 0x41898193, v19
	v_pk_fma_f32 v[20:21], v[20:21], v[160:161], v[140:141]
	v_pk_fma_f32 v[22:23], v[22:23], v[162:163], v[142:143]
	v_exp_f32_e64 v160, -v16
	v_exp_f32_e64 v161, -v17
	v_exp_f32_e64 v162, -v18
	v_exp_f32_e64 v163, -v19
	v_med3_f32 v20, v20, s8, v199
	v_med3_f32 v21, v21, s8, v199
	v_med3_f32 v22, v22, s8, v199
	v_med3_f32 v23, v23, s8, v199
	v_pk_add_f32 v[160:161], v[160:161], 1.0 op_sel_hi:[1,0]
	v_pk_add_f32 v[162:163], v[162:163], 1.0 op_sel_hi:[1,0]
	v_rcp_f32_e32 v160, v160
	v_rcp_f32_e32 v161, v161
	v_rcp_f32_e32 v162, v162
	v_rcp_f32_e32 v163, v163
	v_pk_fma_f32 v[20:21], v[20:21], s[100:101], s[100:101]
	v_pk_fma_f32 v[22:23], v[22:23], s[100:101], s[100:101]
	v_pk_mul_f32 v[16:17], v[16:17], v[160:161]
	v_pk_mul_f32 v[18:19], v[18:19], v[162:163]
	v_pk_mul_f32 v[16:17], v[20:21], v[16:17]
	v_pk_mul_f32 v[18:19], v[22:23], v[18:19]
	v_cvt_pk_fp8_f32 v25, v16, v17
	v_cvt_pk_fp8_f32 v25, v18, v19 op_sel:[0,0,1]
	v_cvt_f32_i32_e32 v0, v0
	v_cvt_f32_i32_e32 v1, v1
	v_cvt_f32_i32_e32 v2, v2
	v_cvt_f32_i32_e32 v3, v3
	v_cvt_f32_i32_e32 v4, v4
	v_cvt_f32_i32_e32 v5, v5
	v_cvt_f32_i32_e32 v6, v6
	v_cvt_f32_i32_e32 v7, v7
	v_pk_mul_f32 v[202:203], v[144:145], v[158:159] op_sel:[0,1] op_sel_hi:[1,1]
	v_pk_mul_f32 v[204:205], v[146:147], v[158:159] op_sel:[0,1] op_sel_hi:[1,1]
	v_pk_fma_f32 v[0:1], v[0:1], v[202:203], v[136:137]
	v_pk_fma_f32 v[2:3], v[2:3], v[204:205], v[138:139]
	v_pk_mul_f32 v[202:203], v[148:149], v[158:159] op_sel:[0,1] op_sel_hi:[1,1]
	v_pk_mul_f32 v[204:205], v[150:151], v[158:159] op_sel:[0,1] op_sel_hi:[1,1]
	v_min_f32_e32 v0, 0x41898193, v0
	v_min_f32_e32 v1, 0x41898193, v1
	v_min_f32_e32 v2, 0x41898193, v2
	v_min_f32_e32 v3, 0x41898193, v3
	v_pk_fma_f32 v[4:5], v[4:5], v[202:203], v[140:141]
	v_pk_fma_f32 v[6:7], v[6:7], v[204:205], v[142:143]
	v_exp_f32_e64 v202, -v0
	v_exp_f32_e64 v203, -v1
	v_exp_f32_e64 v204, -v2
	v_exp_f32_e64 v205, -v3
	v_med3_f32 v4, v4, s8, v199
	v_med3_f32 v5, v5, s8, v199
	v_med3_f32 v6, v6, s8, v199
	v_med3_f32 v7, v7, s8, v199
	v_pk_add_f32 v[202:203], v[202:203], 1.0 op_sel_hi:[1,0]
	v_pk_add_f32 v[204:205], v[204:205], 1.0 op_sel_hi:[1,0]
	v_rcp_f32_e32 v202, v202
	v_rcp_f32_e32 v203, v203
	v_rcp_f32_e32 v204, v204
	v_rcp_f32_e32 v205, v205
	v_pk_fma_f32 v[4:5], v[4:5], s[100:101], s[100:101]
	v_pk_fma_f32 v[6:7], v[6:7], s[100:101], s[100:101]
	v_pk_mul_f32 v[0:1], v[0:1], v[202:203]
	v_pk_mul_f32 v[2:3], v[2:3], v[204:205]
	v_pk_mul_f32 v[0:1], v[4:5], v[0:1]
	v_pk_mul_f32 v[2:3], v[6:7], v[2:3]
	v_cvt_pk_fp8_f32 v27, v0, v1
	v_cvt_pk_fp8_f32 v27, v2, v3 op_sel:[0,0,1]
	s_nop 1
	v_permlane16_swap_b32_e32 v24, v26
	v_permlane16_swap_b32_e32 v25, v27
	v_add_u32_e32 v160, 0x28000, v207
	global_store_dwordx4 v160, v[24:27], s[60:61]
	s_cmp_eq_u32 s38, s89
	s_mov_b64 s[10:11], -1
	s_cbranch_scc1 .LBB0_786
	s_andn2_b64 vcc, exec, s[58:59]
	s_cbranch_vccnz .LBB0_785
	s_barrier
	s_branch .LBB0_785
	s_nop 0
	s_nop 0
	s_nop 0
	s_nop 0
	s_nop 0
	s_nop 0
	s_nop 0
	s_nop 0
	s_nop 0
	s_nop 0
	s_nop 0
	s_nop 0
	s_nop 0
	s_nop 0
	s_nop 0
	s_nop 0
	s_nop 0
	s_nop 0
	s_nop 0
	s_nop 0
	s_nop 0
	s_nop 0
	s_nop 0
	s_nop 0
	s_nop 0
	s_nop 0
	s_nop 0
	s_nop 0
	s_nop 0
	s_nop 0
	s_nop 0
	s_nop 0
	s_nop 0
	s_nop 0
	s_nop 0
	s_nop 0
	s_nop 0
	s_nop 0
	s_nop 0
	s_nop 0
	s_nop 0
	s_nop 0
